# v46 with the out-projection epilogue's residual loads issued as plain loads (no nt hint)
# speedup vs baseline: 1.0084x; 1.0084x over previous
; __device__ __forceinline__ unsigned cvt_pk_bf16(float lo, float hi) { unsigned r; asm volatile("v_cvt_pk_bf16_f32 %0, %1, %2" : "=v"(r) : "v"(lo), "v"(hi)); return r; }
;     __device__ __forceinline__ void operator()(const f32x4 (&acc)[2][2][4][2], const pg8::Unit& u, int wr, int wc, int fr, int fq) const {
;         const int row0 = u.pm * 256 + wr * 64 + fr, col0 = u.pn * 256 + wc * 32 + 8 * fq, b = (u.pm * 256) / S;
;         f32x4 gv[2][2];
; #pragma unroll
;         for (int bj = 0; bj < 2; ++bj)
; #pragma unroll
;             for (int n = 0; n < 2; ++n) gv[bj][n] = *(const f32x4*)(gm + (size_t)b * 6144 + col0 + bj * 128 + n * 4);
;     ...
;         constexpr int PF = 4;
;         if (xin32) {
;             f32x4 xq[PF][2];
; #pragma unroll
;             for (int it = 0; it < PF; ++it) { xq[it][0] = __builtin_nontemporal_load((const f32x4*)(xin32 + EO_OFF(it))); xq[it][1] = __builtin_nontemporal_load((const f32x4*)(xin32 + EO_OFF(it) + 4)); }
; #pragma unroll
;             for (int it = 0; it < 16; ++it) {
;                 const int ai = it >> 3, m = (it >> 1) & 3, bj = it & 1;
;                 const f32x4 x0 = xq[it % PF][0], x1 = xq[it % PF][1];
;                 if (it + PF < 16) { xq[it % PF][0] = __builtin_nontemporal_load((const f32x4*)(xin32 + EO_OFF(it + PF))); xq[it % PF][1] = __builtin_nontemporal_load((const f32x4*)(xin32 + EO_OFF(it + PF) + 4)); }
;                 const f32x4 v0 = x0 + gv[bj][0] * acc[ai][bj][m][0], v1 = x1 + gv[bj][1] * acc[ai][bj][m][1];
;                 u32x4 w; w.x = pg8::cvt_pk_bf16(v0[0], v0[1]); w.y = pg8::cvt_pk_bf16(v0[2], v0[3]); w.z = pg8::cvt_pk_bf16(v1[0], v1[1]); w.w = pg8::cvt_pk_bf16(v1[2], v1[3]);
;                 *(u32x4*)(out + EO_OFF(it)) = w;
;             }
.LBB0_720:
	s_ashr_i32 s15, s43, 31
	s_lshr_b32 s15, s15, 28
	s_add_i32 s15, s43, s15
	s_ashr_i32 s15, s15, 4
	s_mul_hi_i32 s17, s15, 0x6000
	s_mulk_i32 s15, 0x6000
	v_lshl_or_b32 v204, s44, 8, v248
	s_add_u32 s22, s36, s15
	s_addc_u32 s23, s37, s17
	v_lshlrev_b32_e32 v205, 2, v204
	s_lshl_b32 s15, s43, 19
	global_load_dwordx4 v[60:63], v205, s[22:23] offset:16
	global_load_dwordx4 v[64:67], v205, s[22:23]
	global_load_dwordx4 v[52:55], v205, s[22:23] offset:528
	global_load_dwordx4 v[56:59], v205, s[22:23] offset:512
	s_add_u32 s26, s50, s15
	s_addc_u32 s27, s51, 0
	v_lshlrev_b32_e32 v207, 1, v204
	v_lshl_add_u32 v206, v1, 12, v205
	v_lshl_add_u32 v207, v1, 11, v207
	s_andn2_b64 vcc, exec, s[12:13]
	s_cbranch_vccnz .Lop_epi_bf16
	s_lshl_b32 s15, s43, 20
	s_add_u32 s24, s8, s15
	s_addc_u32 s25, s9, 0
	s_add_u32 s28, s24, 0x0
	s_addc_u32 s29, s25, 0
	global_load_dwordx4 v[148:151], v206, s[28:29]
	global_load_dwordx4 v[152:155], v206, s[28:29] offset:16
	global_load_dwordx4 v[156:159], v206, s[28:29] offset:512
	global_load_dwordx4 v[160:163], v206, s[28:29] offset:528
	s_add_u32 s28, s24, 0x10000
	s_addc_u32 s29, s25, 0
	global_load_dwordx4 v[164:167], v206, s[28:29]
	global_load_dwordx4 v[168:171], v206, s[28:29] offset:16
	global_load_dwordx4 v[172:175], v206, s[28:29] offset:512
	global_load_dwordx4 v[176:179], v206, s[28:29] offset:528
	s_add_u32 s28, s24, 0x20000
	s_addc_u32 s29, s25, 0
	global_load_dwordx4 v[180:183], v206, s[28:29]
	global_load_dwordx4 v[184:187], v206, s[28:29] offset:16
	global_load_dwordx4 v[208:211], v206, s[28:29] offset:512
	global_load_dwordx4 v[212:215], v206, s[28:29] offset:528
	s_add_u32 s28, s24, 0x30000
	s_addc_u32 s29, s25, 0
	global_load_dwordx4 v[216:219], v206, s[28:29]
	global_load_dwordx4 v[220:223], v206, s[28:29] offset:16
	global_load_dwordx4 v[224:227], v206, s[28:29] offset:512
	global_load_dwordx4 v[228:231], v206, s[28:29] offset:528
	s_add_u32 s32, s26, 0x0
	s_addc_u32 s33, s27, 0
	s_add_u32 s28, s24, 0x80000
	s_addc_u32 s29, s25, 0
	s_waitcnt vmcnt(14)
	v_pk_fma_f32 v[148:149], v[144:145], v[64:65], v[148:149]
	v_pk_fma_f32 v[150:151], v[146:147], v[66:67], v[150:151]
	v_pk_fma_f32 v[152:153], v[140:141], v[60:61], v[152:153]
	v_pk_fma_f32 v[154:155], v[142:143], v[62:63], v[154:155]
	v_cvt_pk_bf16_f32 v148, v148, v149
	v_cvt_pk_bf16_f32 v149, v150, v151
	v_cvt_pk_bf16_f32 v150, v152, v153
	v_cvt_pk_bf16_f32 v151, v154, v155
	global_store_dwordx4 v207, v[148:151], s[32:33]
	global_load_dwordx4 v[148:151], v206, s[28:29]
	global_load_dwordx4 v[152:155], v206, s[28:29] offset:16
	s_waitcnt vmcnt(15)
	v_pk_fma_f32 v[156:157], v[136:137], v[56:57], v[156:157]
	v_pk_fma_f32 v[158:159], v[138:139], v[58:59], v[158:159]
	v_pk_fma_f32 v[160:161], v[132:133], v[52:53], v[160:161]
	v_pk_fma_f32 v[162:163], v[134:135], v[54:55], v[162:163]
	v_cvt_pk_bf16_f32 v156, v156, v157
	v_cvt_pk_bf16_f32 v157, v158, v159
	v_cvt_pk_bf16_f32 v158, v160, v161
	v_cvt_pk_bf16_f32 v159, v162, v163
	global_store_dwordx4 v207, v[156:159], s[32:33] offset:256
	global_load_dwordx4 v[156:159], v206, s[28:29] offset:512
	global_load_dwordx4 v[160:163], v206, s[28:29] offset:528
	s_add_u32 s32, s26, 0x8000
	s_addc_u32 s33, s27, 0
	s_add_u32 s28, s24, 0x90000
	s_addc_u32 s29, s25, 0
	s_waitcnt vmcnt(16)
	v_pk_fma_f32 v[164:165], v[128:129], v[64:65], v[164:165]
	v_pk_fma_f32 v[166:167], v[130:131], v[66:67], v[166:167]
	v_pk_fma_f32 v[168:169], v[124:125], v[60:61], v[168:169]
	v_pk_fma_f32 v[170:171], v[126:127], v[62:63], v[170:171]
	v_cvt_pk_bf16_f32 v164, v164, v165
	v_cvt_pk_bf16_f32 v165, v166, v167
	v_cvt_pk_bf16_f32 v166, v168, v169
	v_cvt_pk_bf16_f32 v167, v170, v171
	global_store_dwordx4 v207, v[164:167], s[32:33]
	global_load_dwordx4 v[164:167], v206, s[28:29]
	global_load_dwordx4 v[168:171], v206, s[28:29] offset:16
	s_waitcnt vmcnt(17)
	v_pk_fma_f32 v[172:173], v[120:121], v[56:57], v[172:173]
	v_pk_fma_f32 v[174:175], v[122:123], v[58:59], v[174:175]
	v_pk_fma_f32 v[176:177], v[116:117], v[52:53], v[176:177]
	v_pk_fma_f32 v[178:179], v[118:119], v[54:55], v[178:179]
	v_cvt_pk_bf16_f32 v172, v172, v173
	v_cvt_pk_bf16_f32 v173, v174, v175
	v_cvt_pk_bf16_f32 v174, v176, v177
	v_cvt_pk_bf16_f32 v175, v178, v179
	global_store_dwordx4 v207, v[172:175], s[32:33] offset:256
	global_load_dwordx4 v[172:175], v206, s[28:29] offset:512
	global_load_dwordx4 v[176:179], v206, s[28:29] offset:528
	s_add_u32 s32, s26, 0x10000
	s_addc_u32 s33, s27, 0
	s_add_u32 s28, s24, 0xa0000
	s_addc_u32 s29, s25, 0
	s_waitcnt vmcnt(18)
	v_pk_fma_f32 v[180:181], v[112:113], v[64:65], v[180:181]
	v_pk_fma_f32 v[182:183], v[114:115], v[66:67], v[182:183]
	v_pk_fma_f32 v[184:185], v[108:109], v[60:61], v[184:185]
	v_pk_fma_f32 v[186:187], v[110:111], v[62:63], v[186:187]
	v_cvt_pk_bf16_f32 v180, v180, v181
	v_cvt_pk_bf16_f32 v181, v182, v183
	v_cvt_pk_bf16_f32 v182, v184, v185
	v_cvt_pk_bf16_f32 v183, v186, v187
	global_store_dwordx4 v207, v[180:183], s[32:33]
	global_load_dwordx4 v[180:183], v206, s[28:29]
	global_load_dwordx4 v[184:187], v206, s[28:29] offset:16
	s_waitcnt vmcnt(19)
	v_pk_fma_f32 v[208:209], v[104:105], v[56:57], v[208:209]
	v_pk_fma_f32 v[210:211], v[106:107], v[58:59], v[210:211]
	v_pk_fma_f32 v[212:213], v[100:101], v[52:53], v[212:213]
	v_pk_fma_f32 v[214:215], v[102:103], v[54:55], v[214:215]
	v_cvt_pk_bf16_f32 v208, v208, v209
	v_cvt_pk_bf16_f32 v209, v210, v211
	v_cvt_pk_bf16_f32 v210, v212, v213
	v_cvt_pk_bf16_f32 v211, v214, v215
	global_store_dwordx4 v207, v[208:211], s[32:33] offset:256
	global_load_dwordx4 v[208:211], v206, s[28:29] offset:512
	global_load_dwordx4 v[212:215], v206, s[28:29] offset:528
	s_add_u32 s32, s26, 0x18000
	s_addc_u32 s33, s27, 0
	s_add_u32 s28, s24, 0xb0000
	s_addc_u32 s29, s25, 0
	s_waitcnt vmcnt(20)
; __device__ __forceinline__ unsigned cvt_pk_bf16(float lo, float hi) { unsigned r; asm volatile("v_cvt_pk_bf16_f32 %0, %1, %2" : "=v"(r) : "v"(lo), "v"(hi)); return r; }
;     __device__ __forceinline__ void operator()(const f32x4 (&acc)[2][2][4][2], const pg8::Unit& u, int wr, int wc, int fr, int fq) const {
;     ...
;             for (int it = 0; it < 16; ++it) {
;                 const int ai = it >> 3, m = (it >> 1) & 3, bj = it & 1;
;                 const f32x4 x0 = xq[it % PF][0], x1 = xq[it % PF][1];
;                 if (it + PF < 16) { xq[it % PF][0] = __builtin_nontemporal_load((const f32x4*)(xin32 + EO_OFF(it + PF))); xq[it % PF][1] = __builtin_nontemporal_load((const f32x4*)(xin32 + EO_OFF(it + PF) + 4)); }
;                 const f32x4 v0 = x0 + gv[bj][0] * acc[ai][bj][m][0], v1 = x1 + gv[bj][1] * acc[ai][bj][m][1];
;                 u32x4 w; w.x = pg8::cvt_pk_bf16(v0[0], v0[1]); w.y = pg8::cvt_pk_bf16(v0[2], v0[3]); w.z = pg8::cvt_pk_bf16(v1[0], v1[1]); w.w = pg8::cvt_pk_bf16(v1[2], v1[3]);
;                 *(u32x4*)(out + EO_OFF(it)) = w;
;             }
	v_pk_fma_f32 v[216:217], v[96:97], v[64:65], v[216:217]
	v_pk_fma_f32 v[218:219], v[98:99], v[66:67], v[218:219]
	v_pk_fma_f32 v[220:221], v[92:93], v[60:61], v[220:221]
	v_pk_fma_f32 v[222:223], v[94:95], v[62:63], v[222:223]
	v_cvt_pk_bf16_f32 v216, v216, v217
	v_cvt_pk_bf16_f32 v217, v218, v219
	v_cvt_pk_bf16_f32 v218, v220, v221
	v_cvt_pk_bf16_f32 v219, v222, v223
	global_store_dwordx4 v207, v[216:219], s[32:33]
	global_load_dwordx4 v[216:219], v206, s[28:29]
	global_load_dwordx4 v[220:223], v206, s[28:29] offset:16
	s_waitcnt vmcnt(21)
	v_pk_fma_f32 v[224:225], v[88:89], v[56:57], v[224:225]
	v_pk_fma_f32 v[226:227], v[90:91], v[58:59], v[226:227]
	v_pk_fma_f32 v[228:229], v[84:85], v[52:53], v[228:229]
	v_pk_fma_f32 v[230:231], v[86:87], v[54:55], v[230:231]
	v_cvt_pk_bf16_f32 v224, v224, v225
	v_cvt_pk_bf16_f32 v225, v226, v227
	v_cvt_pk_bf16_f32 v226, v228, v229
	v_cvt_pk_bf16_f32 v227, v230, v231
	global_store_dwordx4 v207, v[224:227], s[32:33] offset:256
	global_load_dwordx4 v[224:227], v206, s[28:29] offset:512
	global_load_dwordx4 v[228:231], v206, s[28:29] offset:528
	s_add_u32 s32, s26, 0x40000
	s_addc_u32 s33, s27, 0
	s_waitcnt vmcnt(21)
	v_pk_fma_f32 v[148:149], v[80:81], v[64:65], v[148:149]
	v_pk_fma_f32 v[150:151], v[82:83], v[66:67], v[150:151]
	v_pk_fma_f32 v[152:153], v[76:77], v[60:61], v[152:153]
	v_pk_fma_f32 v[154:155], v[78:79], v[62:63], v[154:155]
	v_cvt_pk_bf16_f32 v148, v148, v149
	v_cvt_pk_bf16_f32 v149, v150, v151
	v_cvt_pk_bf16_f32 v150, v152, v153
	v_cvt_pk_bf16_f32 v151, v154, v155
	global_store_dwordx4 v207, v[148:151], s[32:33]
	s_waitcnt vmcnt(19)
	v_pk_fma_f32 v[156:157], v[72:73], v[56:57], v[156:157]
	v_pk_fma_f32 v[158:159], v[74:75], v[58:59], v[158:159]
	v_pk_fma_f32 v[160:161], v[68:69], v[52:53], v[160:161]
	v_pk_fma_f32 v[162:163], v[70:71], v[54:55], v[162:163]
	v_cvt_pk_bf16_f32 v156, v156, v157
	v_cvt_pk_bf16_f32 v157, v158, v159
	v_cvt_pk_bf16_f32 v158, v160, v161
	v_cvt_pk_bf16_f32 v159, v162, v163
	global_store_dwordx4 v207, v[156:159], s[32:33] offset:256
	s_add_u32 s32, s26, 0x48000
	s_addc_u32 s33, s27, 0
	s_waitcnt vmcnt(17)
	v_pk_fma_f32 v[164:165], v[48:49], v[64:65], v[164:165]
	v_pk_fma_f32 v[166:167], v[50:51], v[66:67], v[166:167]
	v_pk_fma_f32 v[168:169], v[44:45], v[60:61], v[168:169]
	v_pk_fma_f32 v[170:171], v[46:47], v[62:63], v[170:171]
	v_cvt_pk_bf16_f32 v164, v164, v165
	v_cvt_pk_bf16_f32 v165, v166, v167
	v_cvt_pk_bf16_f32 v166, v168, v169
	v_cvt_pk_bf16_f32 v167, v170, v171
	global_store_dwordx4 v207, v[164:167], s[32:33]
	s_waitcnt vmcnt(15)
	v_pk_fma_f32 v[172:173], v[40:41], v[56:57], v[172:173]
	v_pk_fma_f32 v[174:175], v[42:43], v[58:59], v[174:175]
	v_pk_fma_f32 v[176:177], v[36:37], v[52:53], v[176:177]
	v_pk_fma_f32 v[178:179], v[38:39], v[54:55], v[178:179]
	v_cvt_pk_bf16_f32 v172, v172, v173
	v_cvt_pk_bf16_f32 v173, v174, v175
	v_cvt_pk_bf16_f32 v174, v176, v177
	v_cvt_pk_bf16_f32 v175, v178, v179
	global_store_dwordx4 v207, v[172:175], s[32:33] offset:256
	s_add_u32 s32, s26, 0x50000
	s_addc_u32 s33, s27, 0
	s_waitcnt vmcnt(13)
	v_pk_fma_f32 v[180:181], v[30:31], v[64:65], v[180:181]
	v_pk_fma_f32 v[182:183], v[32:33], v[66:67], v[182:183]
	v_pk_fma_f32 v[184:185], v[26:27], v[60:61], v[184:185]
	v_pk_fma_f32 v[186:187], v[28:29], v[62:63], v[186:187]
	v_cvt_pk_bf16_f32 v180, v180, v181
	v_cvt_pk_bf16_f32 v181, v182, v183
	v_cvt_pk_bf16_f32 v182, v184, v185
	v_cvt_pk_bf16_f32 v183, v186, v187
	global_store_dwordx4 v207, v[180:183], s[32:33]
	s_waitcnt vmcnt(11)
	v_pk_fma_f32 v[208:209], v[22:23], v[56:57], v[208:209]
	v_pk_fma_f32 v[210:211], v[24:25], v[58:59], v[210:211]
	v_pk_fma_f32 v[212:213], v[18:19], v[52:53], v[212:213]
	v_pk_fma_f32 v[214:215], v[20:21], v[54:55], v[214:215]
	v_cvt_pk_bf16_f32 v208, v208, v209
	v_cvt_pk_bf16_f32 v209, v210, v211
	v_cvt_pk_bf16_f32 v210, v212, v213
	v_cvt_pk_bf16_f32 v211, v214, v215
	global_store_dwordx4 v207, v[208:211], s[32:33] offset:256
	s_add_u32 s32, s26, 0x58000
	s_addc_u32 s33, s27, 0
	s_waitcnt vmcnt(9)
	v_pk_fma_f32 v[216:217], v[14:15], v[64:65], v[216:217]
	v_pk_fma_f32 v[218:219], v[16:17], v[66:67], v[218:219]
	v_pk_fma_f32 v[220:221], v[10:11], v[60:61], v[220:221]
	v_pk_fma_f32 v[222:223], v[12:13], v[62:63], v[222:223]
	v_cvt_pk_bf16_f32 v216, v216, v217
	v_cvt_pk_bf16_f32 v217, v218, v219
	v_cvt_pk_bf16_f32 v218, v220, v221
	v_cvt_pk_bf16_f32 v219, v222, v223
	global_store_dwordx4 v207, v[216:219], s[32:33]
	s_waitcnt vmcnt(7)
	v_pk_fma_f32 v[224:225], v[6:7], v[56:57], v[224:225]
	v_pk_fma_f32 v[226:227], v[8:9], v[58:59], v[226:227]
	v_pk_fma_f32 v[228:229], v[2:3], v[52:53], v[228:229]
	v_pk_fma_f32 v[230:231], v[4:5], v[54:55], v[230:231]
	v_cvt_pk_bf16_f32 v224, v224, v225
	v_cvt_pk_bf16_f32 v225, v226, v227
	v_cvt_pk_bf16_f32 v226, v228, v229
	v_cvt_pk_bf16_f32 v227, v230, v231
	global_store_dwordx4 v207, v[224:227], s[32:33] offset:256
	s_branch .Lop_epi_done
; __device__ __forceinline__ unsigned cvt_pk_bf16(float lo, float hi) { unsigned r; asm volatile("v_cvt_pk_bf16_f32 %0, %1, %2" : "=v"(r) : "v"(lo), "v"(hi)); return r; }
;     __device__ __forceinline__ void operator()(const f32x4 (&acc)[2][2][4][2], const pg8::Unit& u, int wr, int wc, int fr, int fq) const {
;     ...
;             u32x4 xq[PF];
; #pragma unroll
;             for (int it = 0; it < PF; ++it) xq[it] = __builtin_nontemporal_load((const u32x4*)(xin16 + EO_OFF(it)));
; #pragma unroll
;             for (int it = 0; it < 16; ++it) {
;                 const int ai = it >> 3, m = (it >> 1) & 3, bj = it & 1;
;                 const u32x4 xv = xq[it % PF];
;                 if (it + PF < 16) xq[it % PF] = __builtin_nontemporal_load((const u32x4*)(xin16 + EO_OFF(it + PF)));
;                 const f32x4 x0 = (f32x4){__uint_as_float(xv.x << 16), __uint_as_float(xv.x & 0xffff0000u), __uint_as_float(xv.y << 16), __uint_as_float(xv.y & 0xffff0000u)};
;                 const f32x4 x1 = (f32x4){__uint_as_float(xv.z << 16), __uint_as_float(xv.z & 0xffff0000u), __uint_as_float(xv.w << 16), __uint_as_float(xv.w & 0xffff0000u)};
;                 const f32x4 v0 = x0 + gv[bj][0] * acc[ai][bj][m][0], v1 = x1 + gv[bj][1] * acc[ai][bj][m][1];
;                 u32x4 w; w.x = pg8::cvt_pk_bf16(v0[0], v0[1]); w.y = pg8::cvt_pk_bf16(v0[2], v0[3]); w.z = pg8::cvt_pk_bf16(v1[0], v1[1]); w.w = pg8::cvt_pk_bf16(v1[2], v1[3]);
;                 *(u32x4*)(out + EO_OFF(it)) = w;
;             }
.Lop_epi_bf16:
	s_add_u32 s28, s26, 0x0
	s_addc_u32 s29, s27, 0
	global_load_dwordx4 v[148:151], v207, s[28:29]
	global_load_dwordx4 v[152:155], v207, s[28:29] offset:256
	s_add_u32 s28, s26, 0x8000
	s_addc_u32 s29, s27, 0
	global_load_dwordx4 v[156:159], v207, s[28:29]
	global_load_dwordx4 v[160:163], v207, s[28:29] offset:256
	s_add_u32 s28, s26, 0x10000
	s_addc_u32 s29, s27, 0
	global_load_dwordx4 v[164:167], v207, s[28:29]
	global_load_dwordx4 v[168:171], v207, s[28:29] offset:256
	s_add_u32 s28, s26, 0x18000
	s_addc_u32 s29, s27, 0
	global_load_dwordx4 v[172:175], v207, s[28:29]
	global_load_dwordx4 v[176:179], v207, s[28:29] offset:256
	s_add_u32 s28, s26, 0x40000
	s_addc_u32 s29, s27, 0
	global_load_dwordx4 v[180:183], v207, s[28:29]
	global_load_dwordx4 v[184:187], v207, s[28:29] offset:256
	s_add_u32 s28, s26, 0x48000
	s_addc_u32 s29, s27, 0
	global_load_dwordx4 v[208:211], v207, s[28:29]
	global_load_dwordx4 v[212:215], v207, s[28:29] offset:256
	s_add_u32 s28, s26, 0x50000
	s_addc_u32 s29, s27, 0
	global_load_dwordx4 v[216:219], v207, s[28:29]
	global_load_dwordx4 v[220:223], v207, s[28:29] offset:256
	s_add_u32 s28, s26, 0x58000
	s_addc_u32 s29, s27, 0
	global_load_dwordx4 v[224:227], v207, s[28:29]
	global_load_dwordx4 v[228:231], v207, s[28:29] offset:256
	s_add_u32 s32, s26, 0x0
	s_addc_u32 s33, s27, 0
	s_waitcnt vmcnt(15)
	v_lshlrev_b32_e32 v232, 16, v148
	v_and_b32_e32 v233, 0xffff0000, v148
	v_lshlrev_b32_e32 v234, 16, v149
	v_and_b32_e32 v235, 0xffff0000, v149
	v_lshlrev_b32_e32 v244, 16, v150
	v_and_b32_e32 v245, 0xffff0000, v150
	v_lshlrev_b32_e32 v246, 16, v151
	v_and_b32_e32 v247, 0xffff0000, v151
	v_pk_fma_f32 v[144:145], v[144:145], v[64:65], v[232:233]
	v_pk_fma_f32 v[146:147], v[146:147], v[66:67], v[234:235]
	v_pk_fma_f32 v[140:141], v[140:141], v[60:61], v[244:245]
	v_pk_fma_f32 v[142:143], v[142:143], v[62:63], v[246:247]
	v_cvt_pk_bf16_f32 v148, v144, v145
	v_cvt_pk_bf16_f32 v149, v146, v147
	v_cvt_pk_bf16_f32 v150, v140, v141
	v_cvt_pk_bf16_f32 v151, v142, v143
	global_store_dwordx4 v207, v[148:151], s[32:33]
	s_waitcnt vmcnt(15)
	v_lshlrev_b32_e32 v232, 16, v152
	v_and_b32_e32 v233, 0xffff0000, v152
	v_lshlrev_b32_e32 v234, 16, v153
	v_and_b32_e32 v235, 0xffff0000, v153
	v_lshlrev_b32_e32 v244, 16, v154
	v_and_b32_e32 v245, 0xffff0000, v154
	v_lshlrev_b32_e32 v246, 16, v155
	v_and_b32_e32 v247, 0xffff0000, v155
	v_pk_fma_f32 v[136:137], v[136:137], v[56:57], v[232:233]
	v_pk_fma_f32 v[138:139], v[138:139], v[58:59], v[234:235]
	v_pk_fma_f32 v[132:133], v[132:133], v[52:53], v[244:245]
	v_pk_fma_f32 v[134:135], v[134:135], v[54:55], v[246:247]
	v_cvt_pk_bf16_f32 v152, v136, v137
	v_cvt_pk_bf16_f32 v153, v138, v139
	v_cvt_pk_bf16_f32 v154, v132, v133
	v_cvt_pk_bf16_f32 v155, v134, v135
	global_store_dwordx4 v207, v[152:155], s[32:33] offset:256
	s_add_u32 s32, s26, 0x8000
	s_addc_u32 s33, s27, 0
	s_waitcnt vmcnt(15)
	v_lshlrev_b32_e32 v232, 16, v156
	v_and_b32_e32 v233, 0xffff0000, v156
	v_lshlrev_b32_e32 v234, 16, v157
	v_and_b32_e32 v235, 0xffff0000, v157
	v_lshlrev_b32_e32 v244, 16, v158
	v_and_b32_e32 v245, 0xffff0000, v158
	v_lshlrev_b32_e32 v246, 16, v159
	v_and_b32_e32 v247, 0xffff0000, v159
	v_pk_fma_f32 v[128:129], v[128:129], v[64:65], v[232:233]
	v_pk_fma_f32 v[130:131], v[130:131], v[66:67], v[234:235]
	v_pk_fma_f32 v[124:125], v[124:125], v[60:61], v[244:245]
	v_pk_fma_f32 v[126:127], v[126:127], v[62:63], v[246:247]
	v_cvt_pk_bf16_f32 v156, v128, v129
	v_cvt_pk_bf16_f32 v157, v130, v131
	v_cvt_pk_bf16_f32 v158, v124, v125
	v_cvt_pk_bf16_f32 v159, v126, v127
	global_store_dwordx4 v207, v[156:159], s[32:33]
	s_waitcnt vmcnt(15)
	v_lshlrev_b32_e32 v232, 16, v160
	v_and_b32_e32 v233, 0xffff0000, v160
	v_lshlrev_b32_e32 v234, 16, v161
	v_and_b32_e32 v235, 0xffff0000, v161
	v_lshlrev_b32_e32 v244, 16, v162
	v_and_b32_e32 v245, 0xffff0000, v162
	v_lshlrev_b32_e32 v246, 16, v163
	v_and_b32_e32 v247, 0xffff0000, v163
	v_pk_fma_f32 v[120:121], v[120:121], v[56:57], v[232:233]
	v_pk_fma_f32 v[122:123], v[122:123], v[58:59], v[234:235]
	v_pk_fma_f32 v[116:117], v[116:117], v[52:53], v[244:245]
	v_pk_fma_f32 v[118:119], v[118:119], v[54:55], v[246:247]
	v_cvt_pk_bf16_f32 v160, v120, v121
	v_cvt_pk_bf16_f32 v161, v122, v123
	v_cvt_pk_bf16_f32 v162, v116, v117
	v_cvt_pk_bf16_f32 v163, v118, v119
	global_store_dwordx4 v207, v[160:163], s[32:33] offset:256
	s_add_u32 s32, s26, 0x10000
	s_addc_u32 s33, s27, 0
	s_waitcnt vmcnt(15)
	v_lshlrev_b32_e32 v232, 16, v164
	v_and_b32_e32 v233, 0xffff0000, v164
	v_lshlrev_b32_e32 v234, 16, v165
	v_and_b32_e32 v235, 0xffff0000, v165
	v_lshlrev_b32_e32 v244, 16, v166
	v_and_b32_e32 v245, 0xffff0000, v166
	v_lshlrev_b32_e32 v246, 16, v167
	v_and_b32_e32 v247, 0xffff0000, v167
	v_pk_fma_f32 v[112:113], v[112:113], v[64:65], v[232:233]
	v_pk_fma_f32 v[114:115], v[114:115], v[66:67], v[234:235]
	v_pk_fma_f32 v[108:109], v[108:109], v[60:61], v[244:245]
	v_pk_fma_f32 v[110:111], v[110:111], v[62:63], v[246:247]
	v_cvt_pk_bf16_f32 v164, v112, v113
	v_cvt_pk_bf16_f32 v165, v114, v115
	v_cvt_pk_bf16_f32 v166, v108, v109
	v_cvt_pk_bf16_f32 v167, v110, v111
	global_store_dwordx4 v207, v[164:167], s[32:33]
	s_waitcnt vmcnt(15)
	v_lshlrev_b32_e32 v232, 16, v168
	v_and_b32_e32 v233, 0xffff0000, v168
	v_lshlrev_b32_e32 v234, 16, v169
	v_and_b32_e32 v235, 0xffff0000, v169
	v_lshlrev_b32_e32 v244, 16, v170
	v_and_b32_e32 v245, 0xffff0000, v170
	v_lshlrev_b32_e32 v246, 16, v171
	v_and_b32_e32 v247, 0xffff0000, v171
	v_pk_fma_f32 v[104:105], v[104:105], v[56:57], v[232:233]
	v_pk_fma_f32 v[106:107], v[106:107], v[58:59], v[234:235]
	v_pk_fma_f32 v[100:101], v[100:101], v[52:53], v[244:245]
	v_pk_fma_f32 v[102:103], v[102:103], v[54:55], v[246:247]
	v_cvt_pk_bf16_f32 v168, v104, v105
	v_cvt_pk_bf16_f32 v169, v106, v107
	v_cvt_pk_bf16_f32 v170, v100, v101
	v_cvt_pk_bf16_f32 v171, v102, v103
	global_store_dwordx4 v207, v[168:171], s[32:33] offset:256
	s_add_u32 s32, s26, 0x18000
	s_addc_u32 s33, s27, 0
	s_waitcnt vmcnt(15)
; __device__ __forceinline__ unsigned cvt_pk_bf16(float lo, float hi) { unsigned r; asm volatile("v_cvt_pk_bf16_f32 %0, %1, %2" : "=v"(r) : "v"(lo), "v"(hi)); return r; }
;     __device__ __forceinline__ void operator()(const f32x4 (&acc)[2][2][4][2], const pg8::Unit& u, int wr, int wc, int fr, int fq) const {
;     ...
;             for (int it = 0; it < 16; ++it) {
;                 const int ai = it >> 3, m = (it >> 1) & 3, bj = it & 1;
;                 const u32x4 xv = xq[it % PF];
;                 if (it + PF < 16) xq[it % PF] = __builtin_nontemporal_load((const u32x4*)(xin16 + EO_OFF(it + PF)));
;                 const f32x4 x0 = (f32x4){__uint_as_float(xv.x << 16), __uint_as_float(xv.x & 0xffff0000u), __uint_as_float(xv.y << 16), __uint_as_float(xv.y & 0xffff0000u)};
;                 const f32x4 x1 = (f32x4){__uint_as_float(xv.z << 16), __uint_as_float(xv.z & 0xffff0000u), __uint_as_float(xv.w << 16), __uint_as_float(xv.w & 0xffff0000u)};
;                 const f32x4 v0 = x0 + gv[bj][0] * acc[ai][bj][m][0], v1 = x1 + gv[bj][1] * acc[ai][bj][m][1];
;                 u32x4 w; w.x = pg8::cvt_pk_bf16(v0[0], v0[1]); w.y = pg8::cvt_pk_bf16(v0[2], v0[3]); w.z = pg8::cvt_pk_bf16(v1[0], v1[1]); w.w = pg8::cvt_pk_bf16(v1[2], v1[3]);
;                 *(u32x4*)(out + EO_OFF(it)) = w;
;             }
	v_lshlrev_b32_e32 v232, 16, v172
	v_and_b32_e32 v233, 0xffff0000, v172
	v_lshlrev_b32_e32 v234, 16, v173
	v_and_b32_e32 v235, 0xffff0000, v173
	v_lshlrev_b32_e32 v244, 16, v174
	v_and_b32_e32 v245, 0xffff0000, v174
	v_lshlrev_b32_e32 v246, 16, v175
	v_and_b32_e32 v247, 0xffff0000, v175
	v_pk_fma_f32 v[96:97], v[96:97], v[64:65], v[232:233]
	v_pk_fma_f32 v[98:99], v[98:99], v[66:67], v[234:235]
	v_pk_fma_f32 v[92:93], v[92:93], v[60:61], v[244:245]
	v_pk_fma_f32 v[94:95], v[94:95], v[62:63], v[246:247]
	v_cvt_pk_bf16_f32 v172, v96, v97
	v_cvt_pk_bf16_f32 v173, v98, v99
	v_cvt_pk_bf16_f32 v174, v92, v93
	v_cvt_pk_bf16_f32 v175, v94, v95
	global_store_dwordx4 v207, v[172:175], s[32:33]
	s_waitcnt vmcnt(15)
	v_lshlrev_b32_e32 v232, 16, v176
	v_and_b32_e32 v233, 0xffff0000, v176
	v_lshlrev_b32_e32 v234, 16, v177
	v_and_b32_e32 v235, 0xffff0000, v177
	v_lshlrev_b32_e32 v244, 16, v178
	v_and_b32_e32 v245, 0xffff0000, v178
	v_lshlrev_b32_e32 v246, 16, v179
	v_and_b32_e32 v247, 0xffff0000, v179
	v_pk_fma_f32 v[88:89], v[88:89], v[56:57], v[232:233]
	v_pk_fma_f32 v[90:91], v[90:91], v[58:59], v[234:235]
	v_pk_fma_f32 v[84:85], v[84:85], v[52:53], v[244:245]
	v_pk_fma_f32 v[86:87], v[86:87], v[54:55], v[246:247]
	v_cvt_pk_bf16_f32 v176, v88, v89
	v_cvt_pk_bf16_f32 v177, v90, v91
	v_cvt_pk_bf16_f32 v178, v84, v85
	v_cvt_pk_bf16_f32 v179, v86, v87
	global_store_dwordx4 v207, v[176:179], s[32:33] offset:256
	s_add_u32 s32, s26, 0x40000
	s_addc_u32 s33, s27, 0
	s_waitcnt vmcnt(15)
	v_lshlrev_b32_e32 v232, 16, v180
	v_and_b32_e32 v233, 0xffff0000, v180
	v_lshlrev_b32_e32 v234, 16, v181
	v_and_b32_e32 v235, 0xffff0000, v181
	v_lshlrev_b32_e32 v244, 16, v182
	v_and_b32_e32 v245, 0xffff0000, v182
	v_lshlrev_b32_e32 v246, 16, v183
	v_and_b32_e32 v247, 0xffff0000, v183
	v_pk_fma_f32 v[80:81], v[80:81], v[64:65], v[232:233]
	v_pk_fma_f32 v[82:83], v[82:83], v[66:67], v[234:235]
	v_pk_fma_f32 v[76:77], v[76:77], v[60:61], v[244:245]
	v_pk_fma_f32 v[78:79], v[78:79], v[62:63], v[246:247]
	v_cvt_pk_bf16_f32 v180, v80, v81
	v_cvt_pk_bf16_f32 v181, v82, v83
	v_cvt_pk_bf16_f32 v182, v76, v77
	v_cvt_pk_bf16_f32 v183, v78, v79
	global_store_dwordx4 v207, v[180:183], s[32:33]
	s_waitcnt vmcnt(15)
	v_lshlrev_b32_e32 v232, 16, v184
	v_and_b32_e32 v233, 0xffff0000, v184
	v_lshlrev_b32_e32 v234, 16, v185
	v_and_b32_e32 v235, 0xffff0000, v185
	v_lshlrev_b32_e32 v244, 16, v186
	v_and_b32_e32 v245, 0xffff0000, v186
	v_lshlrev_b32_e32 v246, 16, v187
	v_and_b32_e32 v247, 0xffff0000, v187
	v_pk_fma_f32 v[72:73], v[72:73], v[56:57], v[232:233]
	v_pk_fma_f32 v[74:75], v[74:75], v[58:59], v[234:235]
	v_pk_fma_f32 v[68:69], v[68:69], v[52:53], v[244:245]
	v_pk_fma_f32 v[70:71], v[70:71], v[54:55], v[246:247]
	v_cvt_pk_bf16_f32 v184, v72, v73
	v_cvt_pk_bf16_f32 v185, v74, v75
	v_cvt_pk_bf16_f32 v186, v68, v69
	v_cvt_pk_bf16_f32 v187, v70, v71
	global_store_dwordx4 v207, v[184:187], s[32:33] offset:256
	s_add_u32 s32, s26, 0x48000
	s_addc_u32 s33, s27, 0
	s_waitcnt vmcnt(15)
	v_lshlrev_b32_e32 v232, 16, v208
	v_and_b32_e32 v233, 0xffff0000, v208
	v_lshlrev_b32_e32 v234, 16, v209
	v_and_b32_e32 v235, 0xffff0000, v209
	v_lshlrev_b32_e32 v244, 16, v210
	v_and_b32_e32 v245, 0xffff0000, v210
	v_lshlrev_b32_e32 v246, 16, v211
	v_and_b32_e32 v247, 0xffff0000, v211
	v_pk_fma_f32 v[48:49], v[48:49], v[64:65], v[232:233]
	v_pk_fma_f32 v[50:51], v[50:51], v[66:67], v[234:235]
	v_pk_fma_f32 v[44:45], v[44:45], v[60:61], v[244:245]
	v_pk_fma_f32 v[46:47], v[46:47], v[62:63], v[246:247]
	v_cvt_pk_bf16_f32 v208, v48, v49
	v_cvt_pk_bf16_f32 v209, v50, v51
	v_cvt_pk_bf16_f32 v210, v44, v45
	v_cvt_pk_bf16_f32 v211, v46, v47
	global_store_dwordx4 v207, v[208:211], s[32:33]
	s_waitcnt vmcnt(15)
; __device__ __forceinline__ unsigned cvt_pk_bf16(float lo, float hi) { unsigned r; asm volatile("v_cvt_pk_bf16_f32 %0, %1, %2" : "=v"(r) : "v"(lo), "v"(hi)); return r; }
;     __device__ __forceinline__ void operator()(const f32x4 (&acc)[2][2][4][2], const pg8::Unit& u, int wr, int wc, int fr, int fq) const {
;     ...
;             for (int it = 0; it < 16; ++it) {
;                 const int ai = it >> 3, m = (it >> 1) & 3, bj = it & 1;
;                 const u32x4 xv = xq[it % PF];
;                 if (it + PF < 16) xq[it % PF] = __builtin_nontemporal_load((const u32x4*)(xin16 + EO_OFF(it + PF)));
;                 const f32x4 x0 = (f32x4){__uint_as_float(xv.x << 16), __uint_as_float(xv.x & 0xffff0000u), __uint_as_float(xv.y << 16), __uint_as_float(xv.y & 0xffff0000u)};
;                 const f32x4 x1 = (f32x4){__uint_as_float(xv.z << 16), __uint_as_float(xv.z & 0xffff0000u), __uint_as_float(xv.w << 16), __uint_as_float(xv.w & 0xffff0000u)};
;                 const f32x4 v0 = x0 + gv[bj][0] * acc[ai][bj][m][0], v1 = x1 + gv[bj][1] * acc[ai][bj][m][1];
;                 u32x4 w; w.x = pg8::cvt_pk_bf16(v0[0], v0[1]); w.y = pg8::cvt_pk_bf16(v0[2], v0[3]); w.z = pg8::cvt_pk_bf16(v1[0], v1[1]); w.w = pg8::cvt_pk_bf16(v1[2], v1[3]);
;                 *(u32x4*)(out + EO_OFF(it)) = w;
;             }
	v_lshlrev_b32_e32 v232, 16, v212
	v_and_b32_e32 v233, 0xffff0000, v212
	v_lshlrev_b32_e32 v234, 16, v213
	v_and_b32_e32 v235, 0xffff0000, v213
	v_lshlrev_b32_e32 v244, 16, v214
	v_and_b32_e32 v245, 0xffff0000, v214
	v_lshlrev_b32_e32 v246, 16, v215
	v_and_b32_e32 v247, 0xffff0000, v215
	v_pk_fma_f32 v[40:41], v[40:41], v[56:57], v[232:233]
	v_pk_fma_f32 v[42:43], v[42:43], v[58:59], v[234:235]
	v_pk_fma_f32 v[36:37], v[36:37], v[52:53], v[244:245]
	v_pk_fma_f32 v[38:39], v[38:39], v[54:55], v[246:247]
	v_cvt_pk_bf16_f32 v212, v40, v41
	v_cvt_pk_bf16_f32 v213, v42, v43
	v_cvt_pk_bf16_f32 v214, v36, v37
	v_cvt_pk_bf16_f32 v215, v38, v39
	global_store_dwordx4 v207, v[212:215], s[32:33] offset:256
	s_add_u32 s32, s26, 0x50000
	s_addc_u32 s33, s27, 0
	s_waitcnt vmcnt(15)
	v_lshlrev_b32_e32 v232, 16, v216
	v_and_b32_e32 v233, 0xffff0000, v216
	v_lshlrev_b32_e32 v234, 16, v217
	v_and_b32_e32 v235, 0xffff0000, v217
	v_lshlrev_b32_e32 v244, 16, v218
	v_and_b32_e32 v245, 0xffff0000, v218
	v_lshlrev_b32_e32 v246, 16, v219
	v_and_b32_e32 v247, 0xffff0000, v219
	v_pk_fma_f32 v[30:31], v[30:31], v[64:65], v[232:233]
	v_pk_fma_f32 v[32:33], v[32:33], v[66:67], v[234:235]
	v_pk_fma_f32 v[26:27], v[26:27], v[60:61], v[244:245]
	v_pk_fma_f32 v[28:29], v[28:29], v[62:63], v[246:247]
	v_cvt_pk_bf16_f32 v216, v30, v31
	v_cvt_pk_bf16_f32 v217, v32, v33
	v_cvt_pk_bf16_f32 v218, v26, v27
	v_cvt_pk_bf16_f32 v219, v28, v29
	global_store_dwordx4 v207, v[216:219], s[32:33]
	s_waitcnt vmcnt(15)
	v_lshlrev_b32_e32 v232, 16, v220
	v_and_b32_e32 v233, 0xffff0000, v220
	v_lshlrev_b32_e32 v234, 16, v221
	v_and_b32_e32 v235, 0xffff0000, v221
	v_lshlrev_b32_e32 v244, 16, v222
	v_and_b32_e32 v245, 0xffff0000, v222
	v_lshlrev_b32_e32 v246, 16, v223
	v_and_b32_e32 v247, 0xffff0000, v223
	v_pk_fma_f32 v[22:23], v[22:23], v[56:57], v[232:233]
	v_pk_fma_f32 v[24:25], v[24:25], v[58:59], v[234:235]
	v_pk_fma_f32 v[18:19], v[18:19], v[52:53], v[244:245]
	v_pk_fma_f32 v[20:21], v[20:21], v[54:55], v[246:247]
	v_cvt_pk_bf16_f32 v220, v22, v23
	v_cvt_pk_bf16_f32 v221, v24, v25
	v_cvt_pk_bf16_f32 v222, v18, v19
	v_cvt_pk_bf16_f32 v223, v20, v21
	global_store_dwordx4 v207, v[220:223], s[32:33] offset:256
	s_add_u32 s32, s26, 0x58000
	s_addc_u32 s33, s27, 0
	s_waitcnt vmcnt(15)
	v_lshlrev_b32_e32 v232, 16, v224
	v_and_b32_e32 v233, 0xffff0000, v224
	v_lshlrev_b32_e32 v234, 16, v225
	v_and_b32_e32 v235, 0xffff0000, v225
	v_lshlrev_b32_e32 v244, 16, v226
	v_and_b32_e32 v245, 0xffff0000, v226
	v_lshlrev_b32_e32 v246, 16, v227
	v_and_b32_e32 v247, 0xffff0000, v227
	v_pk_fma_f32 v[14:15], v[14:15], v[64:65], v[232:233]
	v_pk_fma_f32 v[16:17], v[16:17], v[66:67], v[234:235]
	v_pk_fma_f32 v[10:11], v[10:11], v[60:61], v[244:245]
	v_pk_fma_f32 v[12:13], v[12:13], v[62:63], v[246:247]
	v_cvt_pk_bf16_f32 v224, v14, v15
	v_cvt_pk_bf16_f32 v225, v16, v17
	v_cvt_pk_bf16_f32 v226, v10, v11
	v_cvt_pk_bf16_f32 v227, v12, v13
	global_store_dwordx4 v207, v[224:227], s[32:33]
	s_waitcnt vmcnt(15)
	v_lshlrev_b32_e32 v232, 16, v228
	v_and_b32_e32 v233, 0xffff0000, v228
	v_lshlrev_b32_e32 v234, 16, v229
	v_and_b32_e32 v235, 0xffff0000, v229
	v_lshlrev_b32_e32 v244, 16, v230
	v_and_b32_e32 v245, 0xffff0000, v230
	v_lshlrev_b32_e32 v246, 16, v231
	v_and_b32_e32 v247, 0xffff0000, v231
	v_pk_fma_f32 v[6:7], v[6:7], v[56:57], v[232:233]
	v_pk_fma_f32 v[8:9], v[8:9], v[58:59], v[234:235]
	v_pk_fma_f32 v[2:3], v[2:3], v[52:53], v[244:245]
	v_pk_fma_f32 v[4:5], v[4:5], v[54:55], v[246:247]
	v_cvt_pk_bf16_f32 v228, v6, v7
	v_cvt_pk_bf16_f32 v229, v8, v9
	v_cvt_pk_bf16_f32 v230, v2, v3
	v_cvt_pk_bf16_f32 v231, v4, v5
	global_store_dwordx4 v207, v[228:231], s[32:33] offset:256
